# baseline (speedup 1.0000x reference)
.LBB1_4:
	s_or_b64 exec, exec, s[4:5]
	v_lshrrev_b32_e32 v6, 3, v0
	v_mul_u32_u24_e32 v4, 48, v0
	v_and_b32_e32 v6, 60, v6
	v_add3_u32 v4, v2, v4, v6
	s_waitcnt lgkmcnt(0)
	s_barrier
	ds_read_b32 v6, v4
	s_load_dwordx4 s[8:11], s[0:1], 0x40
	s_load_dwordx2 s[12:13], s[0:1], 0x28
	ds_read_b32 v2, v3
	v_lshlrev_b32_e64 v15, v0, 1
	s_lshl_b32 s3, s3, 3
	s_waitcnt lgkmcnt(0)
	v_bitop3_b32 v3, v6, v15, v6 bitop3:0x30
	ds_write_b32 v4, v3
	v_cmp_lt_i32_e32 vcc, -1, v2
	s_and_saveexec_b64 s[4:5], vcc
	v_lshlrev_b32_e64 v3, v2, 1
	v_lshrrev_b32_e32 v2, 3, v2
	v_and_b32_e32 v2, 0x1ffffffc, v2
	ds_or_b32 v2, v3 offset:34816
	s_or_b64 exec, exec, s[4:5]
	v_and_b32_e32 v3, 15, v0
	v_add_u32_e32 v8, s3, v1
	v_lshlrev_b32_e32 v4, 2, v3
	v_lshl_or_b32 v2, v8, 6, v4
	s_load_dwordx2 s[16:17], s[0:1], 0x20
	s_waitcnt lgkmcnt(0)
	s_barrier
	ds_read_b32 v6, v2
	s_lshl_b64 s[4:5], s[14:15], 9
	v_readfirstlane_b32 s22, v8
	s_waitcnt lgkmcnt(0)
	s_branch .LBB1_8
.LBB1_8:
	s_lshr_b32 s23, s22, 5
	s_lshl_b32 s24, -2, s22
	v_cmp_eq_u32_e64 s[44:45], s23, v3
	v_cmp_lt_u32_e32 vcc, s23, v3
	v_and_b32_e32 v9, s24, v6
	v_cndmask_b32_e64 v9, 0, v9, s[44:45]
	v_cndmask_b32_e32 v9, v9, v6, vcc
	v_cmp_ne_u32_e32 vcc, 0, v9
	s_and_b32 s19, vcc_lo, 0xffff
	s_cbranch_scc0 .LBB1_13
	s_ff1_i32_b32 s3, s19
	v_readlane_b32 s15, v9, s3
	s_ff1_i32_b32 s18, s15
	s_lshl_b32 s20, s3, 11
	s_lshl_b32 s21, s18, 6
	s_add_i32 s20, s20, s21
	v_lshl_or_b32 v7, v3, 2, s20
	ds_read_b32 v7, v7
	s_add_i32 s21, s15, -1
	s_and_b32 s15, s15, s21
	s_cbranch_scc1 .Lk2_same
	s_add_i32 s21, s19, -1
	s_and_b32 s19, s19, s21
	s_cbranch_scc0 .Lk2_single
	s_ff1_i32_b32 s3, s19
	v_readlane_b32 s15, v9, s3
.Lk2_same:
	s_ff1_i32_b32 s15, s15
	s_lshl_b32 s20, s3, 5
	s_or_b32 s22, s15, s20
	v_lshl_or_b32 v9, s22, 6, v4
	ds_read_b32 v9, v9
	s_waitcnt lgkmcnt(1)
	v_readlane_b32 s3, v7, s3
	s_lshr_b32 s3, s3, s15
	s_bitcmp0_b32 s3, 0
	s_cselect_b64 vcc, -1, 0
	s_waitcnt lgkmcnt(0)
	v_not_b32_e32 v9, v9
	v_cndmask_b32_e32 v9, -1, v9, vcc
	v_bitop3_b32 v6, v9, v6, v7 bitop3:0x40
	s_branch .LBB1_8
